# attention prologue: the two 6-hop ds_bpermute max butterflies over |g_q|, |g_k| replaced by DPP / permlane-swap all-reduces (max, order-free)
# speedup vs baseline: 1.0044x; 1.0002x over previous
.LBB0_406:
	s_lshl_b64 s[6:7], s[38:39], 2
	s_add_u32 s20, s8, s6
	s_addc_u32 s21, s9, s7
	s_add_u32 s8, s10, s6
	s_addc_u32 s9, s11, s7
	v_cmp_gt_u32_e64 s[6:7], 32, v10
	s_lshl_b32 s10, s25, 9
	s_and_b32 s24, s5, 0xffffffc0
	v_cndmask_b32_e64 v0, v11, v0, s[6:7]
	v_and_b32_e32 v3, 31, v8
	v_add_f32_e32 v0, v0, v12
	s_add_i32 s24, s24, s10
	v_sub_f32_e32 v0, v0, v7
	v_or_b32_e32 v172, s24, v3
	v_pk_add_f32 v[4:5], v[4:5], v[0:1] op_sel_hi:[1,0]
	v_pk_add_f32 v[6:7], v[6:7], v[0:1] op_sel_hi:[1,0]
	v_ashrrev_i32_e32 v173, 31, v172
	v_pk_mul_f32 v[6:7], v[6:7], s[66:67] op_sel_hi:[1,0]
	v_pk_mul_f32 v[4:5], v[4:5], s[66:67] op_sel_hi:[1,0]
	v_lshl_add_u32 v0, v2, 2, 0
	v_lshl_add_u64 v[174:175], s[16:17], 0, v[172:173]
	ds_write_b128 v0, v[4:7] offset:36864
	v_lshlrev_b64 v[4:5], 10, v[174:175]
	v_lshrrev_b32_e32 v49, 5, v10
	v_lshl_add_u64 v[4:5], s[14:15], 0, v[4:5]
	s_lshl_b32 s52, s23, 7
	v_lshl_add_u64 v[4:5], v[4:5], 0, s[52:53]
	v_lshlrev_b32_e32 v0, 4, v49
	v_lshl_add_u64 v[12:13], v[4:5], 0, v[0:1]
	s_mov_b32 s5, 0x5c00000
	v_add_co_u32_e32 v4, vcc, s5, v12
	s_mov_b32 s5, 0x5c08000
	s_nop 0
	v_addc_co_u32_e32 v5, vcc, 0, v13, vcc
	s_mov_b64 s[26:27], 0x5c00000
	v_add_co_u32_e32 v36, vcc, s5, v12
	v_lshl_add_u64 v[32:33], v[12:13], 0, s[26:27]
	s_nop 0
	v_addc_co_u32_e32 v37, vcc, 0, v13, vcc
	s_waitcnt lgkmcnt(0)
	s_barrier

	s_nop 0


	s_nop 0

	s_nop 0

	s_lshl_b32 s4, s4, 13
	v_lshlrev_b32_e32 v2, 4, v10
	s_add_i32 s4, s4, 0
	v_add_u32_e32 v177, s4, v2
	v_lshlrev_b32_e32 v2, 2, v10
	v_ashrrev_i32_e32 v42, 3, v8
	v_ashrrev_i32_e32 v43, 31, v42
	v_and_b32_e32 v54, 7, v8
	v_lshlrev_b32_e32 v46, 4, v54
	v_mov_b32_e32 v47, v1
	v_or_b32_e32 v227, 32, v172
	v_lshlrev_b64 v[50:51], 10, v[42:43]
	v_lshlrev_b32_e32 v55, 2, v49
	s_waitcnt vmcnt(7)
	ds_write_b128 v177, v[60:63] offset:49152
	s_waitcnt vmcnt(6)
	ds_write_b128 v177, v[64:67] offset:53248
	s_waitcnt vmcnt(5)
	ds_write_b128 v177, v[68:71] offset:50176
	s_waitcnt vmcnt(4)
	ds_write_b128 v177, v[72:75] offset:54272
	s_waitcnt vmcnt(3)
	ds_write_b128 v177, v[76:79] offset:51200
	s_waitcnt vmcnt(2)
	ds_write_b128 v177, v[80:83] offset:55296
	s_waitcnt vmcnt(1)
	ds_write_b128 v177, v[84:87] offset:52224
	s_waitcnt vmcnt(0)
	ds_write_b128 v177, v[88:91] offset:56320
	global_load_dword v4, v2, s[20:21]
	v_add_u32_e32 v7, 64, v9
	global_load_dword v2, v2, s[8:9]
	v_xor_b32_e32 v9, 1, v234
	v_cmp_lt_i32_e32 vcc, v9, v7
	s_lshl_b32 s20, s25, 3
	s_add_i32 s20, s20, 8
	v_cndmask_b32_e32 v9, v234, v9, vcc
	v_lshlrev_b32_e32 v9, 2, v9
	s_mov_b64 s[8:9], -1
	v_readfirstlane_b32 s21, v0
	s_waitcnt vmcnt(0)
	v_max_f32_e64 v4, |v4|, |v4|
	v_max_f32_e64 v2, |v2|, |v2|
	s_nop 1
	v_max_f32_dpp v4, v4, v4 quad_perm:[1,0,3,2] row_mask:0xf bank_mask:0xf
	s_nop 1
	v_max_f32_dpp v4, v4, v4 quad_perm:[2,3,0,1] row_mask:0xf bank_mask:0xf
	s_nop 1
	v_max_f32_dpp v4, v4, v4 row_half_mirror row_mask:0xf bank_mask:0xf
	s_nop 1
	v_max_f32_dpp v4, v4, v4 row_ror:8 row_mask:0xf bank_mask:0xf
	v_mov_b32_e32 v6, v4
	s_nop 1
	v_permlane16_swap_b32_e32 v4, v6
	s_nop 0
	v_max_f32_e32 v4, v4, v6
	v_mov_b32_e32 v6, v4
	s_nop 1
	v_permlane32_swap_b32_e32 v4, v6
	s_nop 0
	v_max_f32_e32 v4, v4, v6
	s_nop 1
	v_max_f32_dpp v2, v2, v2 quad_perm:[1,0,3,2] row_mask:0xf bank_mask:0xf
	s_nop 1
	v_max_f32_dpp v2, v2, v2 quad_perm:[2,3,0,1] row_mask:0xf bank_mask:0xf
	s_nop 1
	v_max_f32_dpp v2, v2, v2 row_half_mirror row_mask:0xf bank_mask:0xf
	s_nop 1
	v_max_f32_dpp v2, v2, v2 row_ror:8 row_mask:0xf bank_mask:0xf
	v_mov_b32_e32 v5, v2
	s_nop 1
	v_permlane16_swap_b32_e32 v2, v5
	s_nop 0
	v_max_f32_e32 v2, v2, v5
	v_mov_b32_e32 v5, v2
	s_nop 1
	v_permlane32_swap_b32_e32 v2, v5
	s_nop 0
	v_max_f32_e32 v2, v2, v5
	v_xor_b32_e32 v5, 32, v234
	v_cmp_lt_i32_e32 vcc, v5, v7
	s_nop 1
	v_cndmask_b32_e32 v5, v234, v5, vcc
	v_lshlrev_b32_e32 v226, 2, v5
	v_mul_f32_e32 v4, 0x413c5bb7, v4
	v_mul_f32_e32 v48, v2, v4
	v_lshl_add_u64 v[4:5], s[16:17], 0, v[42:43]
	v_lshlrev_b64 v[4:5], 10, v[4:5]
	v_lshl_add_u64 v[4:5], s[14:15], 0, v[4:5]
	v_readfirstlane_b32 s4, v48
	v_lshl_add_u64 v[4:5], v[4:5], 0, s[52:53]
	s_cmp_gt_u32 s4, 0x421fffff
	v_lshl_add_u64 v[4:5], v[4:5], 0, v[46:47]
	s_mov_b64 s[4:5], 0x7c00000
	v_lshl_add_u64 v[40:41], v[4:5], 0, s[4:5]
	v_lshlrev_b32_e32 v2, 4, v8
	s_movk_i32 s4, 0x90
	v_mul_lo_u32 v43, v42, s4
	v_mul_u32_u24_e32 v47, 0x90, v3
	v_and_b32_e32 v38, 0x70, v2
	s_cbranch_scc0 .LBB0_420
	global_load_dwordx4 v[34:37], v[40:41], off
	v_mul_lo_u32 v228, v42, s4
	v_lshlrev_b32_e32 v230, 4, v49
	s_add_i32 s4, 0, 0x9000
	v_add_u32_e32 v56, s4, v230
	s_lshl_b64 s[4:5], s[18:19], 21
	v_lshl_add_u64 v[44:45], s[4:5], 0, v[50:51]
	v_or3_b32 v44, v44, s52, v38
	v_mul_u32_u24_e32 v231, 0x90, v3
	v_lshl_add_u64 v[2:3], s[14:15], 0, v[44:45]
	s_mov_b64 s[4:5], 0x7c10000
	v_lshlrev_b32_e32 v229, 4, v54
	s_or_b32 s11, s24, 63
	s_or_b32 s21, s24, 31
	v_lshlrev_b32_e32 v176, 2, v49
	v_mov_b32_e32 v39, v1
	v_lshl_add_u64 v[52:53], v[2:3], 0, s[4:5]
	s_add_i32 s4, s10, 0x200
	v_mov_b32_e32 v58, 0xf149f2ca
	s_mov_b32 s5, 0
	s_mov_b32 s8, 1
	v_mov_b32_e32 v57, 0xf149f2ca
	s_branch .LBB0_410
